# grid barrier: follower workgroups poll the top-level generation word directly; per-XCD relay (leader atomic + extra poll round trip) dropped in all 21 barrier instances
# speedup vs baseline: 1.0037x; 1.0037x over previous
; __device__ __forceinline__ unsigned xb_ld(unsigned* p)              { return __hip_atomic_load(p, __ATOMIC_RELAXED, __HIP_MEMORY_SCOPE_AGENT); }
; __device__ __forceinline__ unsigned xb_add(unsigned* p, unsigned v) { return __hip_atomic_fetch_add(p, v, __ATOMIC_RELAXED, __HIP_MEMORY_SCOPE_AGENT); }
; #define XB_SPIN(cond, bar) do { unsigned _sp = 0; while (cond) { __builtin_amdgcn_s_sleep(1); \
;     if ((++_sp & 255u) == 0u) { if (xb_ld(&(bar)[XB_TMO])) break; if (_sp > XB_SPIN_CAP) { atomicAdd(&(bar)[XB_TMO], 1u); break; } } } } while (0)
; __device__ __forceinline__ void xcd_barrier(const XcdBarrier& b) {
;     ...
;         const unsigned old = xb_add(&bar[XB_XSUB(b.x)], 1u);
;         const unsigned gen = old / nloc;
;         if (old + 1u == (gen + 1u) * nloc) {
;             __builtin_amdgcn_fence(__ATOMIC_RELEASE, "agent");
;             asm volatile("s_waitcnt vmcnt(0)" ::: "memory");
;             const unsigned og = xb_add(&bar[XB_TOP], 1u);
;             const unsigned tg = og / nx;
;             if (og + 1u == (tg + 1u) * nx) xb_add(&bar[XB_TOPGEN], 1u);
;             else XB_SPIN(xb_ld(&bar[XB_TOPGEN]) == tg, bar);
;             __builtin_amdgcn_fence(__ATOMIC_ACQUIRE, "agent");
;             xb_add(&bar[XB_XGEN(b.x)], 1u);
;             asm volatile("s_waitcnt vmcnt(0)" ::: "memory");
;         } else {
;             XB_SPIN(xb_ld(&bar[XB_XGEN(b.x)]) == gen, bar);
.LBB0_184:
	s_or_b64 exec, exec, s[12:13]
	v_cvt_f32_u32_e32 v5, v3
	s_waitcnt vmcnt(0)
	v_readfirstlane_b32 s0, v4
	v_sub_u32_e32 v4, 0, v3
	v_rcp_iflag_f32_e32 v5, v5
	v_add_u32_e32 v6, s0, v2
	v_mul_f32_e32 v5, 0x4f7ffffe, v5
	v_cvt_u32_f32_e32 v5, v5
	v_mul_lo_u32 v2, v4, v5
	v_mul_hi_u32 v2, v5, v2
	v_add_u32_e32 v2, v5, v2
	v_mul_hi_u32 v2, v6, v2
	v_mul_lo_u32 v4, v2, v3
	v_sub_u32_e32 v4, v6, v4
	v_add_u32_e32 v5, 1, v2
	v_cmp_ge_u32_e32 vcc, v4, v3
	s_nop 1
	v_cndmask_b32_e32 v2, v2, v5, vcc
	v_sub_u32_e32 v5, v4, v3
	v_cndmask_b32_e32 v4, v4, v5, vcc
	v_add_u32_e32 v5, 1, v2
	v_cmp_ge_u32_e32 vcc, v4, v3
	v_add_u32_e32 v4, 1, v6
	s_nop 0
	v_cndmask_b32_e32 v2, v2, v5, vcc
	v_mul_lo_u32 v5, v3, v2
	v_add_u32_e32 v3, v5, v3
	v_cmp_ne_u32_e32 vcc, v4, v3
	s_and_saveexec_b64 s[0:1], vcc
	s_xor_b64 s[10:11], exec, s[0:1]
	s_cbranch_execz .LBB0_198
	s_waitcnt lgkmcnt(0)
	s_add_u32 s16, s52, 0x7500
	s_addc_u32 s17, s53, 0
	v_mov_b32_e32 v1, 0
	global_load_dword v1, v1, s[16:17] sc1
	s_waitcnt vmcnt(0)
	v_cmp_eq_u32_e32 vcc, v1, v2
	s_and_saveexec_b64 s[12:13], vcc
	s_cbranch_execz .LBB0_197
	s_add_u32 s14, s52, 0x4200
	s_addc_u32 s15, s53, 0
	s_mov_b32 s0, 1
	s_mov_b64 s[18:19], 0
	v_mov_b32_e32 v1, 0
	s_branch .LBB0_188

; __device__ __forceinline__ unsigned xb_ld(unsigned* p)              { return __hip_atomic_load(p, __ATOMIC_RELAXED, __HIP_MEMORY_SCOPE_AGENT); }
; __device__ __forceinline__ unsigned xb_add(unsigned* p, unsigned v) { return __hip_atomic_fetch_add(p, v, __ATOMIC_RELAXED, __HIP_MEMORY_SCOPE_AGENT); }
; #define XB_SPIN(cond, bar) do { unsigned _sp = 0; while (cond) { __builtin_amdgcn_s_sleep(1); \
;     if ((++_sp & 255u) == 0u) { if (xb_ld(&(bar)[XB_TMO])) break; if (_sp > XB_SPIN_CAP) { atomicAdd(&(bar)[XB_TMO], 1u); break; } } } } while (0)
; __device__ __forceinline__ void xcd_barrier(const XcdBarrier& b) {
;     ...
;             const unsigned og = xb_add(&bar[XB_TOP], 1u);
;             const unsigned tg = og / nx;
;             if (og + 1u == (tg + 1u) * nx) xb_add(&bar[XB_TOPGEN], 1u);
;             else XB_SPIN(xb_ld(&bar[XB_TOPGEN]) == tg, bar);
;             __builtin_amdgcn_fence(__ATOMIC_ACQUIRE, "agent");
;             xb_add(&bar[XB_XGEN(b.x)], 1u);
;             asm volatile("s_waitcnt vmcnt(0)" ::: "memory");
.LBB0_215:
	s_or_b64 exec, exec, s[10:11]
	s_mov_b64 s[10:11], exec
	v_mbcnt_lo_u32_b32 v1, s10, 0
	v_mbcnt_hi_u32_b32 v1, s11, v1
	v_cmp_eq_u32_e32 vcc, 0, v1
	s_waitcnt vmcnt(0)
	buffer_inv sc1
	s_and_saveexec_b64 s[12:13], vcc
	s_cbranch_execz .LBB0_217
	s_bcnt1_i32_b64 s0, s[10:11]
	v_mov_b32_e32 v1, 0x2000
	v_mov_b32_e32 v2, s0
.LBB0_217:
	s_or_b64 exec, exec, s[12:13]
	s_waitcnt vmcnt(0)

; __device__ __forceinline__ unsigned xb_ld(unsigned* p)              { return __hip_atomic_load(p, __ATOMIC_RELAXED, __HIP_MEMORY_SCOPE_AGENT); }
; __device__ __forceinline__ unsigned xb_add(unsigned* p, unsigned v) { return __hip_atomic_fetch_add(p, v, __ATOMIC_RELAXED, __HIP_MEMORY_SCOPE_AGENT); }
; #define XB_SPIN(cond, bar) do { unsigned _sp = 0; while (cond) { __builtin_amdgcn_s_sleep(1); \
;     if ((++_sp & 255u) == 0u) { if (xb_ld(&(bar)[XB_TMO])) break; if (_sp > XB_SPIN_CAP) { atomicAdd(&(bar)[XB_TMO], 1u); break; } } } } while (0)
; __device__ __forceinline__ void xcd_barrier(const XcdBarrier& b) {
;     ...
;             const unsigned og = xb_add(&bar[XB_TOP], 1u);
;             const unsigned tg = og / nx;
;             if (og + 1u == (tg + 1u) * nx) xb_add(&bar[XB_TOPGEN], 1u);
;             else XB_SPIN(xb_ld(&bar[XB_TOPGEN]) == tg, bar);
;             __builtin_amdgcn_fence(__ATOMIC_ACQUIRE, "agent");
;             xb_add(&bar[XB_XGEN(b.x)], 1u);
;             asm volatile("s_waitcnt vmcnt(0)" ::: "memory");
.LBB0_723:
	s_or_b64 exec, exec, s[10:11]
	s_mov_b64 s[10:11], exec
	v_mbcnt_lo_u32_b32 v1, s10, 0
	v_mbcnt_hi_u32_b32 v1, s11, v1
	v_cmp_eq_u32_e32 vcc, 0, v1
	s_waitcnt vmcnt(0)
	buffer_inv sc1
	s_and_saveexec_b64 s[12:13], vcc
	s_cbranch_execz .LBB0_725
	s_bcnt1_i32_b64 s0, s[10:11]
	v_mov_b32_e32 v1, 0x2000
	v_mov_b32_e32 v2, s0
.LBB0_725:
	s_or_b64 exec, exec, s[12:13]
	s_waitcnt vmcnt(0)

; __device__ __forceinline__ unsigned xb_ld(unsigned* p)              { return __hip_atomic_load(p, __ATOMIC_RELAXED, __HIP_MEMORY_SCOPE_AGENT); }
; __device__ __forceinline__ unsigned xb_add(unsigned* p, unsigned v) { return __hip_atomic_fetch_add(p, v, __ATOMIC_RELAXED, __HIP_MEMORY_SCOPE_AGENT); }
; #define XB_SPIN(cond, bar) do { unsigned _sp = 0; while (cond) { __builtin_amdgcn_s_sleep(1); \
;     if ((++_sp & 255u) == 0u) { if (xb_ld(&(bar)[XB_TMO])) break; if (_sp > XB_SPIN_CAP) { atomicAdd(&(bar)[XB_TMO], 1u); break; } } } } while (0)
; __device__ __forceinline__ void xcd_barrier(const XcdBarrier& b) {
;     ...
;             const unsigned og = xb_add(&bar[XB_TOP], 1u);
;             const unsigned tg = og / nx;
;             if (og + 1u == (tg + 1u) * nx) xb_add(&bar[XB_TOPGEN], 1u);
;             else XB_SPIN(xb_ld(&bar[XB_TOPGEN]) == tg, bar);
;             __builtin_amdgcn_fence(__ATOMIC_ACQUIRE, "agent");
;             xb_add(&bar[XB_XGEN(b.x)], 1u);
;             asm volatile("s_waitcnt vmcnt(0)" ::: "memory");
.LBB0_880:
	s_or_b64 exec, exec, s[10:11]
	s_mov_b64 s[10:11], exec
	v_mbcnt_lo_u32_b32 v1, s10, 0
	v_mbcnt_hi_u32_b32 v1, s11, v1
	v_cmp_eq_u32_e32 vcc, 0, v1
	s_waitcnt vmcnt(0)
	buffer_inv sc1
	s_and_saveexec_b64 s[12:13], vcc
	s_cbranch_execz .LBB0_882
	s_bcnt1_i32_b64 s0, s[10:11]
	v_mov_b32_e32 v1, 0x2000
	v_mov_b32_e32 v2, s0
.LBB0_882:
	s_or_b64 exec, exec, s[12:13]
	s_waitcnt vmcnt(0)

; __device__ __forceinline__ unsigned xb_ld(unsigned* p)              { return __hip_atomic_load(p, __ATOMIC_RELAXED, __HIP_MEMORY_SCOPE_AGENT); }
; __device__ __forceinline__ unsigned xb_add(unsigned* p, unsigned v) { return __hip_atomic_fetch_add(p, v, __ATOMIC_RELAXED, __HIP_MEMORY_SCOPE_AGENT); }
; #define XB_SPIN(cond, bar) do { unsigned _sp = 0; while (cond) { __builtin_amdgcn_s_sleep(1); \
;     if ((++_sp & 255u) == 0u) { if (xb_ld(&(bar)[XB_TMO])) break; if (_sp > XB_SPIN_CAP) { atomicAdd(&(bar)[XB_TMO], 1u); break; } } } } while (0)
; __device__ __forceinline__ void xcd_barrier(const XcdBarrier& b) {
;     ...
;             const unsigned og = xb_add(&bar[XB_TOP], 1u);
;             const unsigned tg = og / nx;
;             if (og + 1u == (tg + 1u) * nx) xb_add(&bar[XB_TOPGEN], 1u);
;             else XB_SPIN(xb_ld(&bar[XB_TOPGEN]) == tg, bar);
;             __builtin_amdgcn_fence(__ATOMIC_ACQUIRE, "agent");
;             xb_add(&bar[XB_XGEN(b.x)], 1u);
;             asm volatile("s_waitcnt vmcnt(0)" ::: "memory");
.LBB0_943:
	s_or_b64 exec, exec, s[10:11]
	s_mov_b64 s[10:11], exec
	v_mbcnt_lo_u32_b32 v1, s10, 0
	v_mbcnt_hi_u32_b32 v1, s11, v1
	v_cmp_eq_u32_e32 vcc, 0, v1
	s_waitcnt vmcnt(0)
	buffer_inv sc1
	s_and_saveexec_b64 s[12:13], vcc
	s_cbranch_execz .LBB0_945
	s_bcnt1_i32_b64 s0, s[10:11]
	v_mov_b32_e32 v1, 0x2000
	v_mov_b32_e32 v2, s0
.LBB0_945:
	s_or_b64 exec, exec, s[12:13]
	s_waitcnt vmcnt(0)

; __device__ __forceinline__ unsigned xb_ld(unsigned* p)              { return __hip_atomic_load(p, __ATOMIC_RELAXED, __HIP_MEMORY_SCOPE_AGENT); }
; __device__ __forceinline__ unsigned xb_add(unsigned* p, unsigned v) { return __hip_atomic_fetch_add(p, v, __ATOMIC_RELAXED, __HIP_MEMORY_SCOPE_AGENT); }
; #define XB_SPIN(cond, bar) do { unsigned _sp = 0; while (cond) { __builtin_amdgcn_s_sleep(1); \
;     if ((++_sp & 255u) == 0u) { if (xb_ld(&(bar)[XB_TMO])) break; if (_sp > XB_SPIN_CAP) { atomicAdd(&(bar)[XB_TMO], 1u); break; } } } } while (0)
; __device__ __forceinline__ void xcd_barrier(const XcdBarrier& b) {
;     ...
;             const unsigned og = xb_add(&bar[XB_TOP], 1u);
;             const unsigned tg = og / nx;
;             if (og + 1u == (tg + 1u) * nx) xb_add(&bar[XB_TOPGEN], 1u);
;             else XB_SPIN(xb_ld(&bar[XB_TOPGEN]) == tg, bar);
;             __builtin_amdgcn_fence(__ATOMIC_ACQUIRE, "agent");
;             xb_add(&bar[XB_XGEN(b.x)], 1u);
;             asm volatile("s_waitcnt vmcnt(0)" ::: "memory");
.LBB0_1021:
	s_or_b64 exec, exec, s[10:11]
	s_mov_b64 s[10:11], exec
	v_mbcnt_lo_u32_b32 v1, s10, 0
	v_mbcnt_hi_u32_b32 v1, s11, v1
	v_cmp_eq_u32_e32 vcc, 0, v1
	s_waitcnt vmcnt(0)
	buffer_inv sc1
	s_and_saveexec_b64 s[12:13], vcc
	s_cbranch_execz .LBB0_1023
	s_bcnt1_i32_b64 s0, s[10:11]
	v_mov_b32_e32 v1, 0x2000
	v_mov_b32_e32 v2, s0
.LBB0_1023:
	s_or_b64 exec, exec, s[12:13]
	s_waitcnt vmcnt(0)

; __device__ __forceinline__ unsigned xb_ld(unsigned* p)              { return __hip_atomic_load(p, __ATOMIC_RELAXED, __HIP_MEMORY_SCOPE_AGENT); }
; __device__ __forceinline__ unsigned xb_add(unsigned* p, unsigned v) { return __hip_atomic_fetch_add(p, v, __ATOMIC_RELAXED, __HIP_MEMORY_SCOPE_AGENT); }
; #define XB_SPIN(cond, bar) do { unsigned _sp = 0; while (cond) { __builtin_amdgcn_s_sleep(1); \
;     if ((++_sp & 255u) == 0u) { if (xb_ld(&(bar)[XB_TMO])) break; if (_sp > XB_SPIN_CAP) { atomicAdd(&(bar)[XB_TMO], 1u); break; } } } } while (0)
; __device__ __forceinline__ void xcd_barrier(const XcdBarrier& b) {
;     ...
;             const unsigned og = xb_add(&bar[XB_TOP], 1u);
;             const unsigned tg = og / nx;
;             if (og + 1u == (tg + 1u) * nx) xb_add(&bar[XB_TOPGEN], 1u);
;             else XB_SPIN(xb_ld(&bar[XB_TOPGEN]) == tg, bar);
;             __builtin_amdgcn_fence(__ATOMIC_ACQUIRE, "agent");
;             xb_add(&bar[XB_XGEN(b.x)], 1u);
;             asm volatile("s_waitcnt vmcnt(0)" ::: "memory");
.LBB0_1218:
	s_or_b64 exec, exec, s[10:11]
	s_mov_b64 s[10:11], exec
	v_mbcnt_lo_u32_b32 v1, s10, 0
	v_mbcnt_hi_u32_b32 v1, s11, v1
	v_cmp_eq_u32_e32 vcc, 0, v1
	s_waitcnt vmcnt(0)
	buffer_inv sc1
	s_and_saveexec_b64 s[12:13], vcc
	s_cbranch_execz .LBB0_1220
	s_bcnt1_i32_b64 s0, s[10:11]
	v_mov_b32_e32 v1, 0x2000
	v_mov_b32_e32 v2, s0
.LBB0_1220:
	s_or_b64 exec, exec, s[12:13]
	s_waitcnt vmcnt(0)

; __device__ __forceinline__ unsigned xb_ld(unsigned* p)              { return __hip_atomic_load(p, __ATOMIC_RELAXED, __HIP_MEMORY_SCOPE_AGENT); }
; __device__ __forceinline__ unsigned xb_add(unsigned* p, unsigned v) { return __hip_atomic_fetch_add(p, v, __ATOMIC_RELAXED, __HIP_MEMORY_SCOPE_AGENT); }
; #define XB_SPIN(cond, bar) do { unsigned _sp = 0; while (cond) { __builtin_amdgcn_s_sleep(1); \
;     if ((++_sp & 255u) == 0u) { if (xb_ld(&(bar)[XB_TMO])) break; if (_sp > XB_SPIN_CAP) { atomicAdd(&(bar)[XB_TMO], 1u); break; } } } } while (0)
; __device__ __forceinline__ void xcd_barrier(const XcdBarrier& b) {
;     ...
;             const unsigned og = xb_add(&bar[XB_TOP], 1u);
;             const unsigned tg = og / nx;
;             if (og + 1u == (tg + 1u) * nx) xb_add(&bar[XB_TOPGEN], 1u);
;             else XB_SPIN(xb_ld(&bar[XB_TOPGEN]) == tg, bar);
;             __builtin_amdgcn_fence(__ATOMIC_ACQUIRE, "agent");
;             xb_add(&bar[XB_XGEN(b.x)], 1u);
;             asm volatile("s_waitcnt vmcnt(0)" ::: "memory");
.LBB0_1299:
	s_or_b64 exec, exec, s[10:11]
	s_mov_b64 s[10:11], exec
	v_mbcnt_lo_u32_b32 v1, s10, 0
	v_mbcnt_hi_u32_b32 v1, s11, v1
	v_cmp_eq_u32_e32 vcc, 0, v1
	s_waitcnt vmcnt(0)
	buffer_inv sc1
	s_and_saveexec_b64 s[12:13], vcc
	s_cbranch_execz .LBB0_1301
	s_bcnt1_i32_b64 s0, s[10:11]
	v_mov_b32_e32 v1, 0x2000
	v_mov_b32_e32 v2, s0
.LBB0_1301:
	s_or_b64 exec, exec, s[12:13]
	s_waitcnt vmcnt(0)

; __device__ __forceinline__ unsigned xb_ld(unsigned* p)              { return __hip_atomic_load(p, __ATOMIC_RELAXED, __HIP_MEMORY_SCOPE_AGENT); }
; __device__ __forceinline__ unsigned xb_add(unsigned* p, unsigned v) { return __hip_atomic_fetch_add(p, v, __ATOMIC_RELAXED, __HIP_MEMORY_SCOPE_AGENT); }
; #define XB_SPIN(cond, bar) do { unsigned _sp = 0; while (cond) { __builtin_amdgcn_s_sleep(1); \
;     if ((++_sp & 255u) == 0u) { if (xb_ld(&(bar)[XB_TMO])) break; if (_sp > XB_SPIN_CAP) { atomicAdd(&(bar)[XB_TMO], 1u); break; } } } } while (0)
; __device__ __forceinline__ void xcd_barrier(const XcdBarrier& b) {
;     ...
;             const unsigned og = xb_add(&bar[XB_TOP], 1u);
;             const unsigned tg = og / nx;
;             if (og + 1u == (tg + 1u) * nx) xb_add(&bar[XB_TOPGEN], 1u);
;             else XB_SPIN(xb_ld(&bar[XB_TOPGEN]) == tg, bar);
;             __builtin_amdgcn_fence(__ATOMIC_ACQUIRE, "agent");
;             xb_add(&bar[XB_XGEN(b.x)], 1u);
;             asm volatile("s_waitcnt vmcnt(0)" ::: "memory");
.LBB0_1377:
	s_or_b64 exec, exec, s[10:11]
	s_mov_b64 s[10:11], exec
	v_mbcnt_lo_u32_b32 v1, s10, 0
	v_mbcnt_hi_u32_b32 v1, s11, v1
	v_cmp_eq_u32_e32 vcc, 0, v1
	s_waitcnt vmcnt(0)
	buffer_inv sc1
	s_and_saveexec_b64 s[12:13], vcc
	s_cbranch_execz .LBB0_1379
	s_bcnt1_i32_b64 s0, s[10:11]
	v_mov_b32_e32 v1, 0x2000
	v_mov_b32_e32 v2, s0
.LBB0_1379:
	s_or_b64 exec, exec, s[12:13]
	s_waitcnt vmcnt(0)

; __device__ __forceinline__ unsigned xb_ld(unsigned* p)              { return __hip_atomic_load(p, __ATOMIC_RELAXED, __HIP_MEMORY_SCOPE_AGENT); }
; __device__ __forceinline__ unsigned xb_add(unsigned* p, unsigned v) { return __hip_atomic_fetch_add(p, v, __ATOMIC_RELAXED, __HIP_MEMORY_SCOPE_AGENT); }
; #define XB_SPIN(cond, bar) do { unsigned _sp = 0; while (cond) { __builtin_amdgcn_s_sleep(1); \
;     if ((++_sp & 255u) == 0u) { if (xb_ld(&(bar)[XB_TMO])) break; if (_sp > XB_SPIN_CAP) { atomicAdd(&(bar)[XB_TMO], 1u); break; } } } } while (0)
; __device__ __forceinline__ void xcd_barrier(const XcdBarrier& b) {
;     ...
;             const unsigned og = xb_add(&bar[XB_TOP], 1u);
;             const unsigned tg = og / nx;
;             if (og + 1u == (tg + 1u) * nx) xb_add(&bar[XB_TOPGEN], 1u);
;             else XB_SPIN(xb_ld(&bar[XB_TOPGEN]) == tg, bar);
;             __builtin_amdgcn_fence(__ATOMIC_ACQUIRE, "agent");
;             xb_add(&bar[XB_XGEN(b.x)], 1u);
;             asm volatile("s_waitcnt vmcnt(0)" ::: "memory");
.LBB0_1927:
	s_or_b64 exec, exec, s[10:11]
	s_mov_b64 s[10:11], exec
	v_mbcnt_lo_u32_b32 v1, s10, 0
	v_mbcnt_hi_u32_b32 v1, s11, v1
	v_cmp_eq_u32_e32 vcc, 0, v1
	s_waitcnt vmcnt(0)
	buffer_inv sc1
	s_and_saveexec_b64 s[12:13], vcc
	s_cbranch_execz .LBB0_1929
	s_bcnt1_i32_b64 s0, s[10:11]
	v_mov_b32_e32 v1, 0x2000
	v_mov_b32_e32 v2, s0
.LBB0_1929:
	s_or_b64 exec, exec, s[12:13]
	s_waitcnt vmcnt(0)

; __device__ __forceinline__ unsigned xb_ld(unsigned* p)              { return __hip_atomic_load(p, __ATOMIC_RELAXED, __HIP_MEMORY_SCOPE_AGENT); }
; __device__ __forceinline__ unsigned xb_add(unsigned* p, unsigned v) { return __hip_atomic_fetch_add(p, v, __ATOMIC_RELAXED, __HIP_MEMORY_SCOPE_AGENT); }
; #define XB_SPIN(cond, bar) do { unsigned _sp = 0; while (cond) { __builtin_amdgcn_s_sleep(1); \
;     if ((++_sp & 255u) == 0u) { if (xb_ld(&(bar)[XB_TMO])) break; if (_sp > XB_SPIN_CAP) { atomicAdd(&(bar)[XB_TMO], 1u); break; } } } } while (0)
; __device__ __forceinline__ void xcd_barrier(const XcdBarrier& b) {
;     ...
;             const unsigned og = xb_add(&bar[XB_TOP], 1u);
;             const unsigned tg = og / nx;
;             if (og + 1u == (tg + 1u) * nx) xb_add(&bar[XB_TOPGEN], 1u);
;             else XB_SPIN(xb_ld(&bar[XB_TOPGEN]) == tg, bar);
;             __builtin_amdgcn_fence(__ATOMIC_ACQUIRE, "agent");
;             xb_add(&bar[XB_XGEN(b.x)], 1u);
;             asm volatile("s_waitcnt vmcnt(0)" ::: "memory");
.LBB0_2019:
	s_or_b64 exec, exec, s[10:11]
	s_mov_b64 s[10:11], exec
	v_mbcnt_lo_u32_b32 v1, s10, 0
	v_mbcnt_hi_u32_b32 v1, s11, v1
	v_cmp_eq_u32_e32 vcc, 0, v1
	s_waitcnt vmcnt(0)
	buffer_inv sc1
	s_and_saveexec_b64 s[12:13], vcc
	s_cbranch_execz .LBB0_2021
	s_bcnt1_i32_b64 s0, s[10:11]
	v_mov_b32_e32 v1, 0x2000
	v_mov_b32_e32 v2, s0
.LBB0_2021:
	s_or_b64 exec, exec, s[12:13]
	s_waitcnt vmcnt(0)

; __device__ __forceinline__ unsigned xb_ld(unsigned* p)              { return __hip_atomic_load(p, __ATOMIC_RELAXED, __HIP_MEMORY_SCOPE_AGENT); }
; __device__ __forceinline__ unsigned xb_add(unsigned* p, unsigned v) { return __hip_atomic_fetch_add(p, v, __ATOMIC_RELAXED, __HIP_MEMORY_SCOPE_AGENT); }
; #define XB_SPIN(cond, bar) do { unsigned _sp = 0; while (cond) { __builtin_amdgcn_s_sleep(1); \
;     if ((++_sp & 255u) == 0u) { if (xb_ld(&(bar)[XB_TMO])) break; if (_sp > XB_SPIN_CAP) { atomicAdd(&(bar)[XB_TMO], 1u); break; } } } } while (0)
; __device__ __forceinline__ void xcd_barrier(const XcdBarrier& b) {
;     ...
;             const unsigned og = xb_add(&bar[XB_TOP], 1u);
;             const unsigned tg = og / nx;
;             if (og + 1u == (tg + 1u) * nx) xb_add(&bar[XB_TOPGEN], 1u);
;             else XB_SPIN(xb_ld(&bar[XB_TOPGEN]) == tg, bar);
;             __builtin_amdgcn_fence(__ATOMIC_ACQUIRE, "agent");
;             xb_add(&bar[XB_XGEN(b.x)], 1u);
;             asm volatile("s_waitcnt vmcnt(0)" ::: "memory");
.LBB0_2086:
	s_or_b64 exec, exec, s[10:11]
	s_mov_b64 s[10:11], exec
	v_mbcnt_lo_u32_b32 v1, s10, 0
	v_mbcnt_hi_u32_b32 v1, s11, v1
	v_cmp_eq_u32_e32 vcc, 0, v1
	s_waitcnt vmcnt(0)
	buffer_inv sc1
	s_and_saveexec_b64 s[12:13], vcc
	s_cbranch_execz .LBB0_2088
	s_bcnt1_i32_b64 s0, s[10:11]
	v_mov_b32_e32 v1, 0x2000
	v_mov_b32_e32 v2, s0
.LBB0_2088:
	s_or_b64 exec, exec, s[12:13]
	s_waitcnt vmcnt(0)

; __device__ __forceinline__ unsigned xb_ld(unsigned* p)              { return __hip_atomic_load(p, __ATOMIC_RELAXED, __HIP_MEMORY_SCOPE_AGENT); }
; __device__ __forceinline__ unsigned xb_add(unsigned* p, unsigned v) { return __hip_atomic_fetch_add(p, v, __ATOMIC_RELAXED, __HIP_MEMORY_SCOPE_AGENT); }
; #define XB_SPIN(cond, bar) do { unsigned _sp = 0; while (cond) { __builtin_amdgcn_s_sleep(1); \
;     if ((++_sp & 255u) == 0u) { if (xb_ld(&(bar)[XB_TMO])) break; if (_sp > XB_SPIN_CAP) { atomicAdd(&(bar)[XB_TMO], 1u); break; } } } } while (0)
; __device__ __forceinline__ void xcd_barrier(const XcdBarrier& b) {
;     ...
;             const unsigned og = xb_add(&bar[XB_TOP], 1u);
;             const unsigned tg = og / nx;
;             if (og + 1u == (tg + 1u) * nx) xb_add(&bar[XB_TOPGEN], 1u);
;             else XB_SPIN(xb_ld(&bar[XB_TOPGEN]) == tg, bar);
;             __builtin_amdgcn_fence(__ATOMIC_ACQUIRE, "agent");
;             xb_add(&bar[XB_XGEN(b.x)], 1u);
;             asm volatile("s_waitcnt vmcnt(0)" ::: "memory");
.LBB0_2288:
	s_or_b64 exec, exec, s[10:11]
	s_mov_b64 s[10:11], exec
	v_mbcnt_lo_u32_b32 v1, s10, 0
	v_mbcnt_hi_u32_b32 v1, s11, v1
	v_cmp_eq_u32_e32 vcc, 0, v1
	s_waitcnt vmcnt(0)
	buffer_inv sc1
	s_and_saveexec_b64 s[12:13], vcc
	s_cbranch_execz .LBB0_2290
	s_bcnt1_i32_b64 s0, s[10:11]
	v_mov_b32_e32 v1, 0x2000
	v_mov_b32_e32 v2, s0
.LBB0_2290:
	s_or_b64 exec, exec, s[12:13]
	s_waitcnt vmcnt(0)

; __device__ __forceinline__ unsigned xb_ld(unsigned* p)              { return __hip_atomic_load(p, __ATOMIC_RELAXED, __HIP_MEMORY_SCOPE_AGENT); }
; __device__ __forceinline__ unsigned xb_add(unsigned* p, unsigned v) { return __hip_atomic_fetch_add(p, v, __ATOMIC_RELAXED, __HIP_MEMORY_SCOPE_AGENT); }
; #define XB_SPIN(cond, bar) do { unsigned _sp = 0; while (cond) { __builtin_amdgcn_s_sleep(1); \
;     if ((++_sp & 255u) == 0u) { if (xb_ld(&(bar)[XB_TMO])) break; if (_sp > XB_SPIN_CAP) { atomicAdd(&(bar)[XB_TMO], 1u); break; } } } } while (0)
; __device__ __forceinline__ void xcd_barrier(const XcdBarrier& b) {
;     ...
;             const unsigned og = xb_add(&bar[XB_TOP], 1u);
;             const unsigned tg = og / nx;
;             if (og + 1u == (tg + 1u) * nx) xb_add(&bar[XB_TOPGEN], 1u);
;             else XB_SPIN(xb_ld(&bar[XB_TOPGEN]) == tg, bar);
;             __builtin_amdgcn_fence(__ATOMIC_ACQUIRE, "agent");
;             xb_add(&bar[XB_XGEN(b.x)], 1u);
;             asm volatile("s_waitcnt vmcnt(0)" ::: "memory");
.LBB0_2445:
	s_or_b64 exec, exec, s[10:11]
	s_mov_b64 s[10:11], exec
	v_mbcnt_lo_u32_b32 v1, s10, 0
	v_mbcnt_hi_u32_b32 v1, s11, v1
	v_cmp_eq_u32_e32 vcc, 0, v1
	s_waitcnt vmcnt(0)
	buffer_inv sc1
	s_and_saveexec_b64 s[12:13], vcc
	s_cbranch_execz .LBB0_2447
	s_bcnt1_i32_b64 s0, s[10:11]
	v_mov_b32_e32 v1, 0x2000
	v_mov_b32_e32 v2, s0
.LBB0_2447:
	s_or_b64 exec, exec, s[12:13]
	s_waitcnt vmcnt(0)

; __device__ __forceinline__ unsigned xb_ld(unsigned* p)              { return __hip_atomic_load(p, __ATOMIC_RELAXED, __HIP_MEMORY_SCOPE_AGENT); }
; __device__ __forceinline__ unsigned xb_add(unsigned* p, unsigned v) { return __hip_atomic_fetch_add(p, v, __ATOMIC_RELAXED, __HIP_MEMORY_SCOPE_AGENT); }
; #define XB_SPIN(cond, bar) do { unsigned _sp = 0; while (cond) { __builtin_amdgcn_s_sleep(1); \
;     if ((++_sp & 255u) == 0u) { if (xb_ld(&(bar)[XB_TMO])) break; if (_sp > XB_SPIN_CAP) { atomicAdd(&(bar)[XB_TMO], 1u); break; } } } } while (0)
; __device__ __forceinline__ void xcd_barrier(const XcdBarrier& b) {
;     ...
;             const unsigned og = xb_add(&bar[XB_TOP], 1u);
;             const unsigned tg = og / nx;
;             if (og + 1u == (tg + 1u) * nx) xb_add(&bar[XB_TOPGEN], 1u);
;             else XB_SPIN(xb_ld(&bar[XB_TOPGEN]) == tg, bar);
;             __builtin_amdgcn_fence(__ATOMIC_ACQUIRE, "agent");
;             xb_add(&bar[XB_XGEN(b.x)], 1u);
;             asm volatile("s_waitcnt vmcnt(0)" ::: "memory");
.LBB0_2508:
	s_or_b64 exec, exec, s[10:11]
	s_mov_b64 s[10:11], exec
	v_mbcnt_lo_u32_b32 v1, s10, 0
	v_mbcnt_hi_u32_b32 v1, s11, v1
	v_cmp_eq_u32_e32 vcc, 0, v1
	s_waitcnt vmcnt(0)
	buffer_inv sc1
	s_and_saveexec_b64 s[12:13], vcc
	s_cbranch_execz .LBB0_2510
	s_bcnt1_i32_b64 s0, s[10:11]
	v_mov_b32_e32 v1, 0x2000
	v_mov_b32_e32 v2, s0
.LBB0_2510:
	s_or_b64 exec, exec, s[12:13]
	s_waitcnt vmcnt(0)

; __device__ __forceinline__ unsigned xb_ld(unsigned* p)              { return __hip_atomic_load(p, __ATOMIC_RELAXED, __HIP_MEMORY_SCOPE_AGENT); }
; __device__ __forceinline__ unsigned xb_add(unsigned* p, unsigned v) { return __hip_atomic_fetch_add(p, v, __ATOMIC_RELAXED, __HIP_MEMORY_SCOPE_AGENT); }
; #define XB_SPIN(cond, bar) do { unsigned _sp = 0; while (cond) { __builtin_amdgcn_s_sleep(1); \
;     if ((++_sp & 255u) == 0u) { if (xb_ld(&(bar)[XB_TMO])) break; if (_sp > XB_SPIN_CAP) { atomicAdd(&(bar)[XB_TMO], 1u); break; } } } } while (0)
; __device__ __forceinline__ void xcd_barrier(const XcdBarrier& b) {
;     ...
;             const unsigned og = xb_add(&bar[XB_TOP], 1u);
;             const unsigned tg = og / nx;
;             if (og + 1u == (tg + 1u) * nx) xb_add(&bar[XB_TOPGEN], 1u);
;             else XB_SPIN(xb_ld(&bar[XB_TOPGEN]) == tg, bar);
;             __builtin_amdgcn_fence(__ATOMIC_ACQUIRE, "agent");
;             xb_add(&bar[XB_XGEN(b.x)], 1u);
;             asm volatile("s_waitcnt vmcnt(0)" ::: "memory");
.LBB0_2586:
	s_or_b64 exec, exec, s[10:11]
	s_mov_b64 s[10:11], exec
	v_mbcnt_lo_u32_b32 v1, s10, 0
	v_mbcnt_hi_u32_b32 v1, s11, v1
	v_cmp_eq_u32_e32 vcc, 0, v1
	s_waitcnt vmcnt(0)
	buffer_inv sc1
	s_and_saveexec_b64 s[12:13], vcc
	s_cbranch_execz .LBB0_2588
	s_bcnt1_i32_b64 s0, s[10:11]
	v_mov_b32_e32 v1, 0x2000
	v_mov_b32_e32 v2, s0
.LBB0_2588:
	s_or_b64 exec, exec, s[12:13]
	s_waitcnt vmcnt(0)

; __device__ __forceinline__ unsigned xb_ld(unsigned* p)              { return __hip_atomic_load(p, __ATOMIC_RELAXED, __HIP_MEMORY_SCOPE_AGENT); }
; __device__ __forceinline__ unsigned xb_add(unsigned* p, unsigned v) { return __hip_atomic_fetch_add(p, v, __ATOMIC_RELAXED, __HIP_MEMORY_SCOPE_AGENT); }
; #define XB_SPIN(cond, bar) do { unsigned _sp = 0; while (cond) { __builtin_amdgcn_s_sleep(1); \
;     if ((++_sp & 255u) == 0u) { if (xb_ld(&(bar)[XB_TMO])) break; if (_sp > XB_SPIN_CAP) { atomicAdd(&(bar)[XB_TMO], 1u); break; } } } } while (0)
; __device__ __forceinline__ void xcd_barrier(const XcdBarrier& b) {
;     ...
;             const unsigned og = xb_add(&bar[XB_TOP], 1u);
;             const unsigned tg = og / nx;
;             if (og + 1u == (tg + 1u) * nx) xb_add(&bar[XB_TOPGEN], 1u);
;             else XB_SPIN(xb_ld(&bar[XB_TOPGEN]) == tg, bar);
;             __builtin_amdgcn_fence(__ATOMIC_ACQUIRE, "agent");
;             xb_add(&bar[XB_XGEN(b.x)], 1u);
;             asm volatile("s_waitcnt vmcnt(0)" ::: "memory");
.LBB0_2783:
	s_or_b64 exec, exec, s[10:11]
	s_mov_b64 s[10:11], exec
	v_mbcnt_lo_u32_b32 v1, s10, 0
	v_mbcnt_hi_u32_b32 v1, s11, v1
	v_cmp_eq_u32_e32 vcc, 0, v1
	s_waitcnt vmcnt(0)
	buffer_inv sc1
	s_and_saveexec_b64 s[12:13], vcc
	s_cbranch_execz .LBB0_2785
	s_bcnt1_i32_b64 s0, s[10:11]
	v_mov_b32_e32 v1, 0x2000
	v_mov_b32_e32 v2, s0
.LBB0_2785:
	s_or_b64 exec, exec, s[12:13]
	s_waitcnt vmcnt(0)

; __device__ __forceinline__ unsigned xb_ld(unsigned* p)              { return __hip_atomic_load(p, __ATOMIC_RELAXED, __HIP_MEMORY_SCOPE_AGENT); }
; __device__ __forceinline__ unsigned xb_add(unsigned* p, unsigned v) { return __hip_atomic_fetch_add(p, v, __ATOMIC_RELAXED, __HIP_MEMORY_SCOPE_AGENT); }
; #define XB_SPIN(cond, bar) do { unsigned _sp = 0; while (cond) { __builtin_amdgcn_s_sleep(1); \
;     if ((++_sp & 255u) == 0u) { if (xb_ld(&(bar)[XB_TMO])) break; if (_sp > XB_SPIN_CAP) { atomicAdd(&(bar)[XB_TMO], 1u); break; } } } } while (0)
; __device__ __forceinline__ void xcd_barrier(const XcdBarrier& b) {
;     ...
;             const unsigned og = xb_add(&bar[XB_TOP], 1u);
;             const unsigned tg = og / nx;
;             if (og + 1u == (tg + 1u) * nx) xb_add(&bar[XB_TOPGEN], 1u);
;             else XB_SPIN(xb_ld(&bar[XB_TOPGEN]) == tg, bar);
;             __builtin_amdgcn_fence(__ATOMIC_ACQUIRE, "agent");
;             xb_add(&bar[XB_XGEN(b.x)], 1u);
;             asm volatile("s_waitcnt vmcnt(0)" ::: "memory");
.LBB0_2864:
	s_or_b64 exec, exec, s[10:11]
	s_mov_b64 s[10:11], exec
	v_mbcnt_lo_u32_b32 v1, s10, 0
	v_mbcnt_hi_u32_b32 v1, s11, v1
	v_cmp_eq_u32_e32 vcc, 0, v1
	s_waitcnt vmcnt(0)
	buffer_inv sc1
	s_and_saveexec_b64 s[12:13], vcc
	s_cbranch_execz .LBB0_2866
	s_bcnt1_i32_b64 s0, s[10:11]
	v_mov_b32_e32 v1, 0x2000
	v_mov_b32_e32 v2, s0
.LBB0_2866:
	s_or_b64 exec, exec, s[12:13]
	s_waitcnt vmcnt(0)

; __device__ __forceinline__ unsigned xb_ld(unsigned* p)              { return __hip_atomic_load(p, __ATOMIC_RELAXED, __HIP_MEMORY_SCOPE_AGENT); }
; __device__ __forceinline__ unsigned xb_add(unsigned* p, unsigned v) { return __hip_atomic_fetch_add(p, v, __ATOMIC_RELAXED, __HIP_MEMORY_SCOPE_AGENT); }
; #define XB_SPIN(cond, bar) do { unsigned _sp = 0; while (cond) { __builtin_amdgcn_s_sleep(1); \
;     if ((++_sp & 255u) == 0u) { if (xb_ld(&(bar)[XB_TMO])) break; if (_sp > XB_SPIN_CAP) { atomicAdd(&(bar)[XB_TMO], 1u); break; } } } } while (0)
; __device__ __forceinline__ void xcd_barrier(const XcdBarrier& b) {
;     ...
;             const unsigned og = xb_add(&bar[XB_TOP], 1u);
;             const unsigned tg = og / nx;
;             if (og + 1u == (tg + 1u) * nx) xb_add(&bar[XB_TOPGEN], 1u);
;             else XB_SPIN(xb_ld(&bar[XB_TOPGEN]) == tg, bar);
;             __builtin_amdgcn_fence(__ATOMIC_ACQUIRE, "agent");
;             xb_add(&bar[XB_XGEN(b.x)], 1u);
;             asm volatile("s_waitcnt vmcnt(0)" ::: "memory");
.LBB0_2942:
	s_or_b64 exec, exec, s[10:11]
	s_mov_b64 s[10:11], exec
	v_mbcnt_lo_u32_b32 v1, s10, 0
	v_mbcnt_hi_u32_b32 v1, s11, v1
	v_cmp_eq_u32_e32 vcc, 0, v1
	s_waitcnt vmcnt(0)
	buffer_inv sc1
	s_and_saveexec_b64 s[12:13], vcc
	s_cbranch_execz .LBB0_2944
	s_bcnt1_i32_b64 s0, s[10:11]
	v_mov_b32_e32 v1, 0x2000
	v_mov_b32_e32 v2, s0
.LBB0_2944:
	s_or_b64 exec, exec, s[12:13]
	s_waitcnt vmcnt(0)

; __device__ __forceinline__ unsigned xb_ld(unsigned* p)              { return __hip_atomic_load(p, __ATOMIC_RELAXED, __HIP_MEMORY_SCOPE_AGENT); }
; __device__ __forceinline__ unsigned xb_add(unsigned* p, unsigned v) { return __hip_atomic_fetch_add(p, v, __ATOMIC_RELAXED, __HIP_MEMORY_SCOPE_AGENT); }
; #define XB_SPIN(cond, bar) do { unsigned _sp = 0; while (cond) { __builtin_amdgcn_s_sleep(1); \
;     if ((++_sp & 255u) == 0u) { if (xb_ld(&(bar)[XB_TMO])) break; if (_sp > XB_SPIN_CAP) { atomicAdd(&(bar)[XB_TMO], 1u); break; } } } } while (0)
; __device__ __forceinline__ void xcd_barrier(const XcdBarrier& b) {
;     ...
;             const unsigned og = xb_add(&bar[XB_TOP], 1u);
;             const unsigned tg = og / nx;
;             if (og + 1u == (tg + 1u) * nx) xb_add(&bar[XB_TOPGEN], 1u);
;             else XB_SPIN(xb_ld(&bar[XB_TOPGEN]) == tg, bar);
;             __builtin_amdgcn_fence(__ATOMIC_ACQUIRE, "agent");
;             xb_add(&bar[XB_XGEN(b.x)], 1u);
;             asm volatile("s_waitcnt vmcnt(0)" ::: "memory");
.LBB0_3155:
	s_or_b64 exec, exec, s[10:11]
	s_mov_b64 s[10:11], exec
	v_mbcnt_lo_u32_b32 v1, s10, 0
	v_mbcnt_hi_u32_b32 v1, s11, v1
	v_cmp_eq_u32_e32 vcc, 0, v1
	s_waitcnt vmcnt(0)
	buffer_inv sc1
	s_and_saveexec_b64 s[12:13], vcc
	s_cbranch_execz .LBB0_3157
	s_bcnt1_i32_b64 s0, s[10:11]
	v_mov_b32_e32 v1, 0x2000
	v_mov_b32_e32 v2, s0
.LBB0_3157:
	s_or_b64 exec, exec, s[12:13]
	s_waitcnt vmcnt(0)

; __device__ __forceinline__ unsigned xb_ld(unsigned* p)              { return __hip_atomic_load(p, __ATOMIC_RELAXED, __HIP_MEMORY_SCOPE_AGENT); }
; __device__ __forceinline__ unsigned xb_add(unsigned* p, unsigned v) { return __hip_atomic_fetch_add(p, v, __ATOMIC_RELAXED, __HIP_MEMORY_SCOPE_AGENT); }
; #define XB_SPIN(cond, bar) do { unsigned _sp = 0; while (cond) { __builtin_amdgcn_s_sleep(1); \
;     if ((++_sp & 255u) == 0u) { if (xb_ld(&(bar)[XB_TMO])) break; if (_sp > XB_SPIN_CAP) { atomicAdd(&(bar)[XB_TMO], 1u); break; } } } } while (0)
; __device__ __forceinline__ void xcd_barrier(const XcdBarrier& b) {
;     ...
;             const unsigned og = xb_add(&bar[XB_TOP], 1u);
;             const unsigned tg = og / nx;
;             if (og + 1u == (tg + 1u) * nx) xb_add(&bar[XB_TOPGEN], 1u);
;             else XB_SPIN(xb_ld(&bar[XB_TOPGEN]) == tg, bar);
;             __builtin_amdgcn_fence(__ATOMIC_ACQUIRE, "agent");
;             xb_add(&bar[XB_XGEN(b.x)], 1u);
;             asm volatile("s_waitcnt vmcnt(0)" ::: "memory");
.LBB0_3247:
	s_or_b64 exec, exec, s[10:11]
	s_mov_b64 s[10:11], exec
	v_mbcnt_lo_u32_b32 v1, s10, 0
	v_mbcnt_hi_u32_b32 v1, s11, v1
	v_cmp_eq_u32_e32 vcc, 0, v1
	s_waitcnt vmcnt(0)
	buffer_inv sc1
	s_and_saveexec_b64 s[12:13], vcc
	s_cbranch_execz .LBB0_3249
	s_bcnt1_i32_b64 s0, s[10:11]
	v_mov_b32_e32 v1, 0x2000
	v_mov_b32_e32 v2, s0
.LBB0_3249:
	s_or_b64 exec, exec, s[12:13]
	s_waitcnt vmcnt(0)

; __device__ __forceinline__ unsigned xb_ld(unsigned* p)              { return __hip_atomic_load(p, __ATOMIC_RELAXED, __HIP_MEMORY_SCOPE_AGENT); }
; __device__ __forceinline__ unsigned xb_add(unsigned* p, unsigned v) { return __hip_atomic_fetch_add(p, v, __ATOMIC_RELAXED, __HIP_MEMORY_SCOPE_AGENT); }
; #define XB_SPIN(cond, bar) do { unsigned _sp = 0; while (cond) { __builtin_amdgcn_s_sleep(1); \
;     if ((++_sp & 255u) == 0u) { if (xb_ld(&(bar)[XB_TMO])) break; if (_sp > XB_SPIN_CAP) { atomicAdd(&(bar)[XB_TMO], 1u); break; } } } } while (0)
; __device__ __forceinline__ void xcd_barrier(const XcdBarrier& b) {
;     ...
;         const unsigned old = xb_add(&bar[XB_XSUB(b.x)], 1u);
;         const unsigned gen = old / nloc;
;         if (old + 1u == (gen + 1u) * nloc) {
;             __builtin_amdgcn_fence(__ATOMIC_RELEASE, "agent");
;             asm volatile("s_waitcnt vmcnt(0)" ::: "memory");
;             const unsigned og = xb_add(&bar[XB_TOP], 1u);
;             const unsigned tg = og / nx;
;             if (og + 1u == (tg + 1u) * nx) xb_add(&bar[XB_TOPGEN], 1u);
;             else XB_SPIN(xb_ld(&bar[XB_TOPGEN]) == tg, bar);
;             __builtin_amdgcn_fence(__ATOMIC_ACQUIRE, "agent");
;             xb_add(&bar[XB_XGEN(b.x)], 1u);
;             asm volatile("s_waitcnt vmcnt(0)" ::: "memory");
;         } else {
;             XB_SPIN(xb_ld(&bar[XB_XGEN(b.x)]) == gen, bar);
.LBB0_3283:
	s_or_b64 exec, exec, s[6:7]
	v_cvt_f32_u32_e32 v4, v2
	s_waitcnt vmcnt(0)
	v_readfirstlane_b32 s4, v3
	v_sub_u32_e32 v3, 0, v2
	v_rcp_iflag_f32_e32 v4, v4
	v_add_u32_e32 v5, s4, v1
	v_mul_f32_e32 v4, 0x4f7ffffe, v4
	v_cvt_u32_f32_e32 v4, v4
	v_mul_lo_u32 v1, v3, v4
	v_mul_hi_u32 v1, v4, v1
	v_add_u32_e32 v1, v4, v1
	v_mul_hi_u32 v1, v5, v1
	v_mul_lo_u32 v3, v1, v2
	v_sub_u32_e32 v3, v5, v3
	v_add_u32_e32 v4, 1, v1
	v_cmp_ge_u32_e32 vcc, v3, v2
	s_nop 1
	v_cndmask_b32_e32 v1, v1, v4, vcc
	v_sub_u32_e32 v4, v3, v2
	v_cndmask_b32_e32 v3, v3, v4, vcc
	v_add_u32_e32 v4, 1, v1
	v_cmp_ge_u32_e32 vcc, v3, v2
	v_add_u32_e32 v3, 1, v5
	s_nop 0
	v_cndmask_b32_e32 v1, v1, v4, vcc
	v_mul_lo_u32 v4, v2, v1
	v_add_u32_e32 v2, v4, v2
	v_cmp_ne_u32_e32 vcc, v3, v2
	s_and_saveexec_b64 s[4:5], vcc
	s_xor_b64 s[4:5], exec, s[4:5]
	s_cbranch_execz .LBB0_3297
	s_waitcnt lgkmcnt(0)
	s_add_u32 s10, s52, 0x7500
	s_addc_u32 s11, s53, 0
	v_mov_b32_e32 v0, 0
	global_load_dword v0, v0, s[10:11] sc1
	s_waitcnt vmcnt(0)
	v_cmp_eq_u32_e32 vcc, v0, v1
	s_and_saveexec_b64 s[6:7], vcc
	s_cbranch_execz .LBB0_3296
	s_add_u32 s8, s52, 0x4200
	s_addc_u32 s9, s53, 0
	s_mov_b32 s22, 1
	s_mov_b64 s[12:13], 0
	v_mov_b32_e32 v0, 0
	s_branch .LBB0_3287

; __device__ __forceinline__ unsigned xb_ld(unsigned* p)              { return __hip_atomic_load(p, __ATOMIC_RELAXED, __HIP_MEMORY_SCOPE_AGENT); }
; __device__ __forceinline__ unsigned xb_add(unsigned* p, unsigned v) { return __hip_atomic_fetch_add(p, v, __ATOMIC_RELAXED, __HIP_MEMORY_SCOPE_AGENT); }
; #define XB_SPIN(cond, bar) do { unsigned _sp = 0; while (cond) { __builtin_amdgcn_s_sleep(1); \
;     if ((++_sp & 255u) == 0u) { if (xb_ld(&(bar)[XB_TMO])) break; if (_sp > XB_SPIN_CAP) { atomicAdd(&(bar)[XB_TMO], 1u); break; } } } } while (0)
; __device__ __forceinline__ void xcd_barrier(const XcdBarrier& b) {
;     ...
;             const unsigned og = xb_add(&bar[XB_TOP], 1u);
;             const unsigned tg = og / nx;
;             if (og + 1u == (tg + 1u) * nx) xb_add(&bar[XB_TOPGEN], 1u);
;             else XB_SPIN(xb_ld(&bar[XB_TOPGEN]) == tg, bar);
;             __builtin_amdgcn_fence(__ATOMIC_ACQUIRE, "agent");
;             xb_add(&bar[XB_XGEN(b.x)], 1u);
;             asm volatile("s_waitcnt vmcnt(0)" ::: "memory");
.LBB0_3314:
	s_or_b64 exec, exec, s[4:5]
	s_mov_b64 s[4:5], exec
	v_mbcnt_lo_u32_b32 v0, s4, 0
	v_mbcnt_hi_u32_b32 v0, s5, v0
	v_cmp_eq_u32_e32 vcc, 0, v0
	s_waitcnt vmcnt(0)
	buffer_inv sc1
	s_and_saveexec_b64 s[6:7], vcc
	s_cbranch_execz .LBB0_3316
	s_bcnt1_i32_b64 s4, s[4:5]
	v_mov_b32_e32 v0, 0x2000
	v_mov_b32_e32 v1, s4
.LBB0_3316:
	s_or_b64 exec, exec, s[6:7]
	s_waitcnt vmcnt(0)
